# speedup vs baseline: 1.0327x; 1.0034x over previous
.Lk1_nowarm0:
	s_and_b32 s15, s2, 7
	s_lshl_b32 s15, s15, 2
	s_lshr_b32 s17, s2, 6
	s_add_u32 s15, s15, s17
	s_bfe_u32 s16, s2, 0x30003
	s_mul_i32 s17, s16, 0x271
	v_add_u32_e32 v2, s17, v0
	v_lshlrev_b32_e32 v1, 2, v2
	s_movk_i32 s17, 0x271
	v_cmp_gt_u32_e32 vcc, s17, v0
	s_and_b64 exec, exec, vcc
	s_mov_b64 s[18:19], exec
	s_lshr_b32 s21, s21, 6
	s_movk_i32 s13, 0x4e20
	s_mov_b32 s14, 0x3fb8aa3b
	s_mov_b32 s12, 0
	s_mov_b32 s10, 0x13d620
	s_mov_b32 s11, 0x20000
	s_mul_i32 s17, s15, 0x13d620
	s_mul_hi_u32 s20, s15, 0x13d620
	s_mov_b32 s40, 0
	s_add_u32 s41, s40, s13
	s_add_u32 s42, s41, s13
	s_add_u32 s43, s42, s13
	s_add_u32 s44, s43, s13
	s_add_u32 s45, s44, s13
	s_add_u32 s46, s45, s13
	s_add_u32 s47, s46, s13
	s_add_u32 s48, s47, s13
	s_add_u32 s49, s48, s13
	s_add_u32 s50, s49, s13
	s_add_u32 s51, s50, s13
	s_add_u32 s52, s51, s13
	s_add_u32 s53, s52, s13
	s_add_u32 s54, s53, s13
	s_add_u32 s55, s54, s13
	s_waitcnt lgkmcnt(0)
	s_add_u32 s8, s4, s17
	s_addc_u32 s9, s5, s20
	s_and_b32 s9, s9, 0xffff
	buffer_load_dword v8, v1, s[8:11], s40 offen nt
	buffer_load_dword v9, v1, s[8:11], s41 offen nt
	buffer_load_dword v10, v1, s[8:11], s42 offen nt
	buffer_load_dword v11, v1, s[8:11], s43 offen nt
	buffer_load_dword v12, v1, s[8:11], s44 offen nt
	buffer_load_dword v13, v1, s[8:11], s45 offen nt
	buffer_load_dword v14, v1, s[8:11], s46 offen nt
	buffer_load_dword v15, v1, s[8:11], s47 offen nt
	buffer_load_dword v16, v1, s[8:11], s48 offen nt
	buffer_load_dword v17, v1, s[8:11], s49 offen nt
	buffer_load_dword v18, v1, s[8:11], s50 offen nt
	buffer_load_dword v19, v1, s[8:11], s51 offen nt
	buffer_load_dword v20, v1, s[8:11], s52 offen nt
	buffer_load_dword v21, v1, s[8:11], s53 offen nt
	buffer_load_dword v22, v1, s[8:11], s54 offen nt
	buffer_load_dword v23, v1, s[8:11], s55 offen nt
	s_add_u32 s8, s8, 0x4e200
	s_addc_u32 s9, s9, 0
	buffer_load_dword v24, v1, s[8:11], s40 offen nt
	buffer_load_dword v25, v1, s[8:11], s41 offen nt
	buffer_load_dword v26, v1, s[8:11], s42 offen nt
	buffer_load_dword v27, v1, s[8:11], s43 offen nt
	buffer_load_dword v28, v1, s[8:11], s44 offen nt
	buffer_load_dword v29, v1, s[8:11], s45 offen nt
	buffer_load_dword v30, v1, s[8:11], s46 offen nt
	buffer_load_dword v31, v1, s[8:11], s47 offen nt
	buffer_load_dword v32, v1, s[8:11], s48 offen nt
	buffer_load_dword v33, v1, s[8:11], s49 offen nt
	buffer_load_dword v34, v1, s[8:11], s50 offen nt
	buffer_load_dword v35, v1, s[8:11], s51 offen nt
	buffer_load_dword v36, v1, s[8:11], s52 offen nt
	buffer_load_dword v37, v1, s[8:11], s53 offen nt
	buffer_load_dword v38, v1, s[8:11], s54 offen nt
	buffer_load_dword v39, v1, s[8:11], s55 offen nt
	s_add_u32 s8, s8, 0x4e200
	s_addc_u32 s9, s9, 0
	buffer_load_dword v40, v1, s[8:11], s40 offen nt
	buffer_load_dword v41, v1, s[8:11], s41 offen nt
	buffer_load_dword v42, v1, s[8:11], s42 offen nt
	buffer_load_dword v43, v1, s[8:11], s43 offen nt
	buffer_load_dword v44, v1, s[8:11], s44 offen nt
	buffer_load_dword v45, v1, s[8:11], s45 offen nt
	buffer_load_dword v46, v1, s[8:11], s46 offen nt
	buffer_load_dword v47, v1, s[8:11], s47 offen nt
	buffer_load_dword v48, v1, s[8:11], s48 offen nt
	buffer_load_dword v49, v1, s[8:11], s49 offen nt
	buffer_load_dword v50, v1, s[8:11], s50 offen nt
	buffer_load_dword v51, v1, s[8:11], s51 offen nt
	buffer_load_dword v52, v1, s[8:11], s52 offen nt
	buffer_load_dword v53, v1, s[8:11], s53 offen nt
	buffer_load_dword v54, v1, s[8:11], s54 offen nt
	buffer_load_dword v55, v1, s[8:11], s55 offen nt
	s_add_u32 s8, s8, 0x4e200
	s_addc_u32 s9, s9, 0
	buffer_load_dword v56, v1, s[8:11], s40 offen nt
	buffer_load_dword v57, v1, s[8:11], s41 offen nt
	buffer_load_dword v58, v1, s[8:11], s42 offen nt
	buffer_load_dword v59, v1, s[8:11], s43 offen nt
	buffer_load_dword v60, v1, s[8:11], s44 offen nt
	buffer_load_dword v61, v1, s[8:11], s45 offen nt
	buffer_load_dword v62, v1, s[8:11], s46 offen nt
	buffer_load_dword v63, v1, s[8:11], s47 offen nt
	buffer_load_dword v64, v1, s[8:11], s48 offen nt
	buffer_load_dword v65, v1, s[8:11], s49 offen nt
	buffer_load_dword v66, v1, s[8:11], s50 offen nt
	v_mul_u32_u24_e32 v3, 0x147b, v2
	v_lshrrev_b32_e32 v3, 19, v3
	v_mul_u32_u24_e32 v98, 0x64, v3
	v_sub_u32_e32 v98, v2, v98
	v_add_u32_e32 v3, -1, v3
	v_add_u32_e32 v98, -1, v98
	s_movk_i32 s17, 0x62
	v_cmp_gt_u32_e64 s[36:37], 48, v3
	v_cmp_gt_u32_e64 s[38:39], s17, v98
	s_mul_i32 s17, s15, 0x1388
	v_add_lshl_u32 v98, v2, s17, 3
	s_and_b64 s[36:37], s[36:37], s[38:39]
	s_waitcnt vmcnt(55)
	buffer_load_dword v67, v1, s[8:11], s51 offen nt
	buffer_load_dword v68, v1, s[8:11], s52 offen nt
	buffer_load_dword v69, v1, s[8:11], s53 offen nt
	buffer_load_dword v70, v1, s[8:11], s54 offen nt
	buffer_load_dword v71, v1, s[8:11], s55 offen nt
	s_add_u32 s8, s8, 0x4e200
	s_addc_u32 s9, s9, 0
	buffer_load_dword v72, v1, s[8:11], s40 offen nt
	s_cmp_lg_u32 s21, 0
	s_cbranch_scc1 .Lk1_nowarmk
	s_and_b32 s30, s0, 0xfffff000
	s_mov_b32 s31, s1
	v_lshlrev_b32_e32 v3, 6, v0
	global_load_dword v95, v3, s[30:31]
